# baseline (speedup 1.0000x reference)
_Z11align_fusedPKfS0_PKiPf:
	s_load_dwordx8 s[4:11], s[0:1], 0x0
	s_and_b32 s3, s2, 7
	s_lshl_b32 s3, s3, 10
	s_lshr_b32 s2, s2, 3
	s_add_i32 s2, s3, s2
	s_mul_i32 s12, s2, 0x5dc0
	v_and_b32_e32 v7, 63, v0
	v_readfirstlane_b32 s13, v0
	v_lshlrev_b32_e32 v1, 4, v7
	v_mul_u32_u24_e32 v3, 12, v7
	s_mul_i32 s18, s13, 96
	s_mul_i32 s3, s13, 6
	s_sub_u32 s3, 0x49c, s3
	v_cmp_gt_u32_e64 s[14:15], s3, v7
	v_add_u32_e32 v2, s18, v1
	v_add_u32_e32 v3, s18, v3
	v_add_u32_e32 v4, 0x600, v3
	s_add_u32 s12, s12, s18
	s_add_u32 s12, s12, 0x800
	s_waitcnt lgkmcnt(0)
	s_add_u32 s4, s4, s12
	s_addc_u32 s5, s5, 0
	s_add_u32 s10, s10, s12
	s_addc_u32 s11, s11, 0
	s_cmp_lg_u32 s13, 0
	s_cbranch_scc1 .Lbulk_waves
	v_lshlrev_b32_e32 v5, 2, v7
	global_load_dword v5, v5, s[8:9]
	global_load_dwordx3 v[44:46], v3, s[6:7] nt
	global_load_dwordx4 v[8:11], v1, s[4:5] offset:-2048 nt
	global_load_dwordx4 v[12:15], v1, s[4:5] offset:-1024 nt
	global_load_dwordx4 v[16:19], v1, s[4:5] offset:0 nt
	global_load_dwordx4 v[20:23], v1, s[4:5] offset:1024 nt
	global_load_dwordx4 v[24:27], v1, s[4:5] offset:2048 nt
	global_load_dwordx4 v[28:31], v1, s[4:5] offset:3072 nt
	s_mov_b32 s20, 0
	s_mov_b32 s21, 0x10000
	s_mov_b32 s22, 0
	s_mov_b32 s23, 0x20000
	s_mov_b32 s24, 0
	s_mov_b32 s25, 0x40000
	s_mov_b32 s26, 0
	s_mov_b32 s27, 0x80000
	s_waitcnt vmcnt(6)
	v_mul_u32_u24_e32 v5, 12, v5
	v_add_f32_dpp v52, v44, v44 quad_perm:[1,0,3,2] row_mask:0xf bank_mask:0xf
	v_add_f32_dpp v53, v45, v45 quad_perm:[1,0,3,2] row_mask:0xf bank_mask:0xf
	v_add_f32_dpp v54, v46, v46 quad_perm:[1,0,3,2] row_mask:0xf bank_mask:0xf
	v_add_f32_dpp v52, v52, v52 quad_perm:[2,3,0,1] row_mask:0xf bank_mask:0xf
	v_add_f32_dpp v53, v53, v53 quad_perm:[2,3,0,1] row_mask:0xf bank_mask:0xf
	v_add_f32_dpp v54, v54, v54 quad_perm:[2,3,0,1] row_mask:0xf bank_mask:0xf
	v_add_f32_dpp v52, v52, v52 row_half_mirror row_mask:0xf bank_mask:0xf
	v_add_f32_dpp v53, v53, v53 row_half_mirror row_mask:0xf bank_mask:0xf
	v_add_f32_dpp v54, v54, v54 row_half_mirror row_mask:0xf bank_mask:0xf
	v_add_f32_dpp v52, v52, v52 row_mirror row_mask:0xf bank_mask:0xf
	v_add_f32_dpp v53, v53, v53 row_mirror row_mask:0xf bank_mask:0xf
	v_add_f32_dpp v54, v54, v54 row_mirror row_mask:0xf bank_mask:0xf
	v_add_f32_dpp v52, v52, v52 row_bcast:15 row_mask:0xa bank_mask:0xf
	v_add_f32_dpp v53, v53, v53 row_bcast:15 row_mask:0xa bank_mask:0xf
	v_add_f32_dpp v54, v54, v54 row_bcast:15 row_mask:0xa bank_mask:0xf
	v_add_f32_dpp v52, v52, v52 row_bcast:31 row_mask:0xc bank_mask:0xf
	v_add_f32_dpp v53, v53, v53 row_bcast:31 row_mask:0xc bank_mask:0xf
	v_add_f32_dpp v54, v54, v54 row_bcast:31 row_mask:0xc bank_mask:0xf
	v_readlane_b32 s28, v52, 63
	v_readlane_b32 s29, v53, 63
	v_readlane_b32 s30, v54, 63
	v_mov_b32_e32 v52, s28
	v_mov_b32_e32 v53, s29
	v_mov_b32_e32 v54, s30
	v_fmac_f32_e32 v44, 0xbc800000, v52
	v_fmac_f32_e32 v45, 0xbc800000, v53
	v_fmac_f32_e32 v46, 0xbc800000, v54
	s_waitcnt vmcnt(0)
	ds_write_b128 v2, v[8:11]
	ds_write_b128 v2, v[12:15] offset:1024
	ds_write_b128 v2, v[16:19] offset:2048
	ds_write_b128 v2, v[20:23] offset:3072
	ds_write_b128 v2, v[24:27] offset:4096
	ds_write_b128 v2, v[28:31] offset:5120
	s_waitcnt lgkmcnt(0)
	s_barrier
	ds_read_b32 v48, v5
	ds_read_b32 v49, v5 offset:4
	ds_read_b32 v50, v5 offset:8
	s_waitcnt lgkmcnt(0)
	v_add_f32_dpp v52, v48, v48 quad_perm:[1,0,3,2] row_mask:0xf bank_mask:0xf
	v_add_f32_dpp v53, v49, v49 quad_perm:[1,0,3,2] row_mask:0xf bank_mask:0xf
	v_add_f32_dpp v54, v50, v50 quad_perm:[1,0,3,2] row_mask:0xf bank_mask:0xf
	v_add_f32_dpp v52, v52, v52 quad_perm:[2,3,0,1] row_mask:0xf bank_mask:0xf
	v_add_f32_dpp v53, v53, v53 quad_perm:[2,3,0,1] row_mask:0xf bank_mask:0xf
	v_add_f32_dpp v54, v54, v54 quad_perm:[2,3,0,1] row_mask:0xf bank_mask:0xf
	v_add_f32_dpp v52, v52, v52 row_half_mirror row_mask:0xf bank_mask:0xf
	v_add_f32_dpp v53, v53, v53 row_half_mirror row_mask:0xf bank_mask:0xf
	v_add_f32_dpp v54, v54, v54 row_half_mirror row_mask:0xf bank_mask:0xf
	v_add_f32_dpp v52, v52, v52 row_mirror row_mask:0xf bank_mask:0xf
	v_add_f32_dpp v53, v53, v53 row_mirror row_mask:0xf bank_mask:0xf
	v_add_f32_dpp v54, v54, v54 row_mirror row_mask:0xf bank_mask:0xf
	v_add_f32_dpp v52, v52, v52 row_bcast:15 row_mask:0xa bank_mask:0xf
	v_add_f32_dpp v53, v53, v53 row_bcast:15 row_mask:0xa bank_mask:0xf
	v_add_f32_dpp v54, v54, v54 row_bcast:15 row_mask:0xa bank_mask:0xf
	v_add_f32_dpp v52, v52, v52 row_bcast:31 row_mask:0xc bank_mask:0xf
	v_add_f32_dpp v53, v53, v53 row_bcast:31 row_mask:0xc bank_mask:0xf
	v_add_f32_dpp v54, v54, v54 row_bcast:31 row_mask:0xc bank_mask:0xf
	v_readlane_b32 s32, v52, 63
	v_readlane_b32 s33, v53, 63
	v_readlane_b32 s34, v54, 63
	v_mov_b32_e32 v52, s32
	v_mov_b32_e32 v53, s33
	v_mov_b32_e32 v54, s34
	v_fmac_f32_e32 v48, 0xbc800000, v52
	v_fmac_f32_e32 v49, 0xbc800000, v53
	v_fmac_f32_e32 v50, 0xbc800000, v54
	v_mul_f32_e32 v52, v48, v44
	v_mul_f32_e32 v53, v48, v45
	v_mul_f32_e32 v54, v48, v46
	v_mul_f32_e32 v55, v49, v44
	v_mul_f32_e32 v56, v49, v45
	v_mul_f32_e32 v57, v49, v46
	v_mul_f32_e32 v58, v50, v44
	v_mul_f32_e32 v59, v50, v45
	v_mul_f32_e32 v60, v50, v46
	v_add_f32_dpp v52, v52, v52 quad_perm:[1,0,3,2] row_mask:0xf bank_mask:0xf
	v_add_f32_dpp v53, v53, v53 quad_perm:[1,0,3,2] row_mask:0xf bank_mask:0xf
	v_add_f32_dpp v54, v54, v54 quad_perm:[1,0,3,2] row_mask:0xf bank_mask:0xf
	v_add_f32_dpp v55, v55, v55 quad_perm:[1,0,3,2] row_mask:0xf bank_mask:0xf
	v_add_f32_dpp v56, v56, v56 quad_perm:[1,0,3,2] row_mask:0xf bank_mask:0xf
	v_add_f32_dpp v57, v57, v57 quad_perm:[1,0,3,2] row_mask:0xf bank_mask:0xf
	v_add_f32_dpp v58, v58, v58 quad_perm:[1,0,3,2] row_mask:0xf bank_mask:0xf
	v_add_f32_dpp v59, v59, v59 quad_perm:[1,0,3,2] row_mask:0xf bank_mask:0xf
	v_add_f32_dpp v60, v60, v60 quad_perm:[1,0,3,2] row_mask:0xf bank_mask:0xf
	v_add_f32_dpp v52, v52, v52 quad_perm:[2,3,0,1] row_mask:0xf bank_mask:0xf
	v_add_f32_dpp v53, v53, v53 quad_perm:[2,3,0,1] row_mask:0xf bank_mask:0xf
	v_add_f32_dpp v54, v54, v54 quad_perm:[2,3,0,1] row_mask:0xf bank_mask:0xf
	v_add_f32_dpp v55, v55, v55 quad_perm:[2,3,0,1] row_mask:0xf bank_mask:0xf
	v_add_f32_dpp v56, v56, v56 quad_perm:[2,3,0,1] row_mask:0xf bank_mask:0xf
	v_add_f32_dpp v57, v57, v57 quad_perm:[2,3,0,1] row_mask:0xf bank_mask:0xf
	v_add_f32_dpp v58, v58, v58 quad_perm:[2,3,0,1] row_mask:0xf bank_mask:0xf
	v_add_f32_dpp v59, v59, v59 quad_perm:[2,3,0,1] row_mask:0xf bank_mask:0xf
	v_add_f32_dpp v60, v60, v60 quad_perm:[2,3,0,1] row_mask:0xf bank_mask:0xf
	v_add_f32_dpp v52, v52, v52 row_half_mirror row_mask:0xf bank_mask:0xf
	v_add_f32_dpp v53, v53, v53 row_half_mirror row_mask:0xf bank_mask:0xf
	v_add_f32_dpp v54, v54, v54 row_half_mirror row_mask:0xf bank_mask:0xf
	v_add_f32_dpp v55, v55, v55 row_half_mirror row_mask:0xf bank_mask:0xf
	v_add_f32_dpp v56, v56, v56 row_half_mirror row_mask:0xf bank_mask:0xf
	v_add_f32_dpp v57, v57, v57 row_half_mirror row_mask:0xf bank_mask:0xf
	v_add_f32_dpp v58, v58, v58 row_half_mirror row_mask:0xf bank_mask:0xf
	v_add_f32_dpp v59, v59, v59 row_half_mirror row_mask:0xf bank_mask:0xf
	v_add_f32_dpp v60, v60, v60 row_half_mirror row_mask:0xf bank_mask:0xf
	v_add_f32_dpp v52, v52, v52 row_mirror row_mask:0xf bank_mask:0xf
	v_add_f32_dpp v53, v53, v53 row_mirror row_mask:0xf bank_mask:0xf
	v_add_f32_dpp v54, v54, v54 row_mirror row_mask:0xf bank_mask:0xf
	v_add_f32_dpp v55, v55, v55 row_mirror row_mask:0xf bank_mask:0xf
	v_add_f32_dpp v56, v56, v56 row_mirror row_mask:0xf bank_mask:0xf
	v_add_f32_dpp v57, v57, v57 row_mirror row_mask:0xf bank_mask:0xf
	v_add_f32_dpp v58, v58, v58 row_mirror row_mask:0xf bank_mask:0xf
	v_add_f32_dpp v59, v59, v59 row_mirror row_mask:0xf bank_mask:0xf
	v_add_f32_dpp v60, v60, v60 row_mirror row_mask:0xf bank_mask:0xf
	v_add_f32_dpp v52, v52, v52 row_bcast:15 row_mask:0xa bank_mask:0xf
	v_add_f32_dpp v53, v53, v53 row_bcast:15 row_mask:0xa bank_mask:0xf
	v_add_f32_dpp v54, v54, v54 row_bcast:15 row_mask:0xa bank_mask:0xf
	v_add_f32_dpp v55, v55, v55 row_bcast:15 row_mask:0xa bank_mask:0xf
	v_add_f32_dpp v56, v56, v56 row_bcast:15 row_mask:0xa bank_mask:0xf
	v_add_f32_dpp v57, v57, v57 row_bcast:15 row_mask:0xa bank_mask:0xf
	v_add_f32_dpp v58, v58, v58 row_bcast:15 row_mask:0xa bank_mask:0xf
	v_add_f32_dpp v59, v59, v59 row_bcast:15 row_mask:0xa bank_mask:0xf
	v_add_f32_dpp v60, v60, v60 row_bcast:15 row_mask:0xa bank_mask:0xf
	v_add_f32_dpp v52, v52, v52 row_bcast:31 row_mask:0xc bank_mask:0xf
	v_add_f32_dpp v53, v53, v53 row_bcast:31 row_mask:0xc bank_mask:0xf
	v_add_f32_dpp v54, v54, v54 row_bcast:31 row_mask:0xc bank_mask:0xf
	v_add_f32_dpp v55, v55, v55 row_bcast:31 row_mask:0xc bank_mask:0xf
	v_add_f32_dpp v56, v56, v56 row_bcast:31 row_mask:0xc bank_mask:0xf
	v_add_f32_dpp v57, v57, v57 row_bcast:31 row_mask:0xc bank_mask:0xf
	v_add_f32_dpp v58, v58, v58 row_bcast:31 row_mask:0xc bank_mask:0xf
	v_add_f32_dpp v59, v59, v59 row_bcast:31 row_mask:0xc bank_mask:0xf
	v_add_f32_dpp v60, v60, v60 row_bcast:31 row_mask:0xc bank_mask:0xf
	v_cndmask_b32_e64 v52, v52, v55, s[22:23]
	v_cndmask_b32_e64 v53, v53, v56, s[22:23]
	v_cndmask_b32_e64 v54, v54, v57, s[22:23]
	v_cndmask_b32_e64 v52, v52, v58, s[24:25]
	v_cndmask_b32_e64 v53, v53, v59, s[24:25]
	v_cndmask_b32_e64 v54, v54, v60, s[24:25]
	v_cndmask_b32_e64 v52, v52, 0, s[26:27]
	v_cndmask_b32_e64 v53, v53, 0, s[26:27]
	v_cndmask_b32_e64 v54, v54, 0, s[26:27]
	v_cndmask_b32_e64 v40, 0, 1.0, s[20:21]
	v_cndmask_b32_e64 v41, 0, 1.0, s[22:23]
	v_cndmask_b32_e64 v42, 0, 1.0, s[24:25]
	v_mul_f32_e32 v55, v52, v52
	v_mul_f32_e32 v56, v53, v53
	v_mul_f32_e32 v57, v52, v53
	v_add_f32_dpp v55, v55, v55 quad_perm:[1,0,3,2] row_mask:0xf bank_mask:0xf
	v_add_f32_dpp v56, v56, v56 quad_perm:[1,0,3,2] row_mask:0xf bank_mask:0xf
	v_add_f32_dpp v57, v57, v57 quad_perm:[1,0,3,2] row_mask:0xf bank_mask:0xf
	v_add_f32_dpp v55, v55, v55 quad_perm:[2,3,0,1] row_mask:0xf bank_mask:0xf
	v_add_f32_dpp v56, v56, v56 quad_perm:[2,3,0,1] row_mask:0xf bank_mask:0xf
	v_add_f32_dpp v57, v57, v57 quad_perm:[2,3,0,1] row_mask:0xf bank_mask:0xf
	v_sub_f32_e32 v60, v56, v55
	v_mul_f32_e32 v58, v57, v57
	v_cmp_gt_f32_e32 vcc, 0, v60
	v_mul_f32_e32 v59, v60, v60
	v_fmac_f32_e32 v59, 4.0, v58
	v_sqrt_f32_e32 v59, v59
	s_nop 0
	v_add_f32_e64 v59, |v60|, v59
	v_add_f32_e32 v59, 0x0da24260, v59
	v_rcp_f32_e32 v59, v59
	v_add_f32_e32 v58, v57, v57
	v_mul_f32_e32 v59, v58, v59
	v_cndmask_b32_e64 v59, v59, -v59, vcc
	v_fma_f32 v58, v59, v59, 1.0
	v_rsq_f32_e32 v61, v58
	s_nop 0
	v_mul_f32_e32 v62, v61, v59
	v_mul_f32_e32 v55, v62, v53
	v_mul_f32_e32 v56, v62, v52
	v_fma_f32 v52, v61, v52, -v55
	v_fma_f32 v53, v61, v53, v56
	v_mul_f32_e32 v55, v52, v52
	v_mul_f32_e32 v56, v54, v54
	v_mul_f32_e32 v57, v52, v54
	v_add_f32_dpp v55, v55, v55 quad_perm:[1,0,3,2] row_mask:0xf bank_mask:0xf
	v_add_f32_dpp v56, v56, v56 quad_perm:[1,0,3,2] row_mask:0xf bank_mask:0xf
	v_add_f32_dpp v57, v57, v57 quad_perm:[1,0,3,2] row_mask:0xf bank_mask:0xf
	v_add_f32_dpp v55, v55, v55 quad_perm:[2,3,0,1] row_mask:0xf bank_mask:0xf
	v_add_f32_dpp v56, v56, v56 quad_perm:[2,3,0,1] row_mask:0xf bank_mask:0xf
	v_add_f32_dpp v57, v57, v57 quad_perm:[2,3,0,1] row_mask:0xf bank_mask:0xf
	v_sub_f32_e32 v60, v56, v55
	v_mul_f32_e32 v58, v57, v57
	v_cmp_gt_f32_e32 vcc, 0, v60
	v_mul_f32_e32 v59, v60, v60
	v_fmac_f32_e32 v59, 4.0, v58
	v_sqrt_f32_e32 v59, v59
	v_mul_f32_e32 v63, v62, v41
	v_mul_f32_e32 v43, v62, v40
	v_fma_f32 v40, v61, v40, -v63
	v_fma_f32 v41, v61, v41, v43
	v_add_f32_e64 v59, |v60|, v59
	v_add_f32_e32 v59, 0x0da24260, v59
	v_rcp_f32_e32 v59, v59
	v_add_f32_e32 v58, v57, v57
	v_mul_f32_e32 v59, v58, v59
	v_cndmask_b32_e64 v59, v59, -v59, vcc
	v_fma_f32 v58, v59, v59, 1.0
	v_rsq_f32_e32 v61, v58
	s_nop 0
	v_mul_f32_e32 v62, v61, v59
	v_mul_f32_e32 v55, v62, v54
	v_mul_f32_e32 v56, v62, v52
	v_fma_f32 v52, v61, v52, -v55
	v_fma_f32 v54, v61, v54, v56
	v_mul_f32_e32 v55, v53, v53
	v_mul_f32_e32 v56, v54, v54
	v_mul_f32_e32 v57, v53, v54
	v_add_f32_dpp v55, v55, v55 quad_perm:[1,0,3,2] row_mask:0xf bank_mask:0xf
	v_add_f32_dpp v56, v56, v56 quad_perm:[1,0,3,2] row_mask:0xf bank_mask:0xf
	v_add_f32_dpp v57, v57, v57 quad_perm:[1,0,3,2] row_mask:0xf bank_mask:0xf
	v_add_f32_dpp v55, v55, v55 quad_perm:[2,3,0,1] row_mask:0xf bank_mask:0xf
	v_add_f32_dpp v56, v56, v56 quad_perm:[2,3,0,1] row_mask:0xf bank_mask:0xf
	v_add_f32_dpp v57, v57, v57 quad_perm:[2,3,0,1] row_mask:0xf bank_mask:0xf
	v_sub_f32_e32 v60, v56, v55
	v_mul_f32_e32 v58, v57, v57
	v_cmp_gt_f32_e32 vcc, 0, v60
	v_mul_f32_e32 v59, v60, v60
	v_fmac_f32_e32 v59, 4.0, v58
	v_sqrt_f32_e32 v59, v59
	v_mul_f32_e32 v63, v62, v42
	v_mul_f32_e32 v43, v62, v40
	v_fma_f32 v40, v61, v40, -v63
	v_fma_f32 v42, v61, v42, v43
	v_add_f32_e64 v59, |v60|, v59
	v_add_f32_e32 v59, 0x0da24260, v59
	v_rcp_f32_e32 v59, v59
	v_add_f32_e32 v58, v57, v57
	v_mul_f32_e32 v59, v58, v59
	v_cndmask_b32_e64 v59, v59, -v59, vcc
	v_fma_f32 v58, v59, v59, 1.0
	v_rsq_f32_e32 v61, v58
	s_nop 0
	v_mul_f32_e32 v62, v61, v59
	v_mul_f32_e32 v55, v62, v54
	v_mul_f32_e32 v56, v62, v53
	v_fma_f32 v53, v61, v53, -v55
	v_fma_f32 v54, v61, v54, v56
	v_mul_f32_e32 v55, v52, v52
	v_mul_f32_e32 v56, v53, v53
	v_mul_f32_e32 v57, v52, v53
	v_add_f32_dpp v55, v55, v55 quad_perm:[1,0,3,2] row_mask:0xf bank_mask:0xf
	v_add_f32_dpp v56, v56, v56 quad_perm:[1,0,3,2] row_mask:0xf bank_mask:0xf
	v_add_f32_dpp v57, v57, v57 quad_perm:[1,0,3,2] row_mask:0xf bank_mask:0xf
	v_add_f32_dpp v55, v55, v55 quad_perm:[2,3,0,1] row_mask:0xf bank_mask:0xf
	v_add_f32_dpp v56, v56, v56 quad_perm:[2,3,0,1] row_mask:0xf bank_mask:0xf
	v_add_f32_dpp v57, v57, v57 quad_perm:[2,3,0,1] row_mask:0xf bank_mask:0xf
	v_sub_f32_e32 v60, v56, v55
	v_mul_f32_e32 v58, v57, v57
	v_cmp_gt_f32_e32 vcc, 0, v60
	v_mul_f32_e32 v59, v60, v60
	v_fmac_f32_e32 v59, 4.0, v58
	v_sqrt_f32_e32 v59, v59
	v_mul_f32_e32 v63, v62, v42
	v_mul_f32_e32 v43, v62, v41
	v_fma_f32 v41, v61, v41, -v63
	v_fma_f32 v42, v61, v42, v43
	v_add_f32_e64 v59, |v60|, v59
	v_add_f32_e32 v59, 0x0da24260, v59
	v_rcp_f32_e32 v59, v59
	v_add_f32_e32 v58, v57, v57
	v_mul_f32_e32 v59, v58, v59
	v_cndmask_b32_e64 v59, v59, -v59, vcc
	v_fma_f32 v58, v59, v59, 1.0
	v_rsq_f32_e32 v61, v58
	s_nop 0
	v_mul_f32_e32 v62, v61, v59
	v_mul_f32_e32 v55, v62, v53
	v_mul_f32_e32 v56, v62, v52
	v_fma_f32 v52, v61, v52, -v55
	v_fma_f32 v53, v61, v53, v56
	v_mul_f32_e32 v55, v52, v52
	v_mul_f32_e32 v56, v54, v54
	v_mul_f32_e32 v57, v52, v54
	v_add_f32_dpp v55, v55, v55 quad_perm:[1,0,3,2] row_mask:0xf bank_mask:0xf
	v_add_f32_dpp v56, v56, v56 quad_perm:[1,0,3,2] row_mask:0xf bank_mask:0xf
	v_add_f32_dpp v57, v57, v57 quad_perm:[1,0,3,2] row_mask:0xf bank_mask:0xf
	v_add_f32_dpp v55, v55, v55 quad_perm:[2,3,0,1] row_mask:0xf bank_mask:0xf
	v_add_f32_dpp v56, v56, v56 quad_perm:[2,3,0,1] row_mask:0xf bank_mask:0xf
	v_add_f32_dpp v57, v57, v57 quad_perm:[2,3,0,1] row_mask:0xf bank_mask:0xf
	v_sub_f32_e32 v60, v56, v55
	v_mul_f32_e32 v58, v57, v57
	v_cmp_gt_f32_e32 vcc, 0, v60
	v_mul_f32_e32 v59, v60, v60
	v_fmac_f32_e32 v59, 4.0, v58
	v_sqrt_f32_e32 v59, v59
	v_mul_f32_e32 v63, v62, v41
	v_mul_f32_e32 v43, v62, v40
	v_fma_f32 v40, v61, v40, -v63
	v_fma_f32 v41, v61, v41, v43
	v_add_f32_e64 v59, |v60|, v59
	v_add_f32_e32 v59, 0x0da24260, v59
	v_rcp_f32_e32 v59, v59
	v_add_f32_e32 v58, v57, v57
	v_mul_f32_e32 v59, v58, v59
	v_cndmask_b32_e64 v59, v59, -v59, vcc
	v_fma_f32 v58, v59, v59, 1.0
	v_rsq_f32_e32 v61, v58
	s_nop 0
	v_mul_f32_e32 v62, v61, v59
	v_mul_f32_e32 v55, v62, v54
	v_mul_f32_e32 v56, v62, v52
	v_fma_f32 v52, v61, v52, -v55
	v_fma_f32 v54, v61, v54, v56
	v_mul_f32_e32 v55, v53, v53
	v_mul_f32_e32 v56, v54, v54
	v_mul_f32_e32 v57, v53, v54
	v_add_f32_dpp v55, v55, v55 quad_perm:[1,0,3,2] row_mask:0xf bank_mask:0xf
	v_add_f32_dpp v56, v56, v56 quad_perm:[1,0,3,2] row_mask:0xf bank_mask:0xf
	v_add_f32_dpp v57, v57, v57 quad_perm:[1,0,3,2] row_mask:0xf bank_mask:0xf
	v_add_f32_dpp v55, v55, v55 quad_perm:[2,3,0,1] row_mask:0xf bank_mask:0xf
	v_add_f32_dpp v56, v56, v56 quad_perm:[2,3,0,1] row_mask:0xf bank_mask:0xf
	v_add_f32_dpp v57, v57, v57 quad_perm:[2,3,0,1] row_mask:0xf bank_mask:0xf
	v_sub_f32_e32 v60, v56, v55
	v_mul_f32_e32 v58, v57, v57
	v_cmp_gt_f32_e32 vcc, 0, v60
	v_mul_f32_e32 v59, v60, v60
	v_fmac_f32_e32 v59, 4.0, v58
	v_sqrt_f32_e32 v59, v59
	v_mul_f32_e32 v63, v62, v42
	v_mul_f32_e32 v43, v62, v40
	v_fma_f32 v40, v61, v40, -v63
	v_fma_f32 v42, v61, v42, v43
	v_add_f32_e64 v59, |v60|, v59
	v_add_f32_e32 v59, 0x0da24260, v59
	v_rcp_f32_e32 v59, v59
	v_add_f32_e32 v58, v57, v57
	v_mul_f32_e32 v59, v58, v59
	v_cndmask_b32_e64 v59, v59, -v59, vcc
	v_fma_f32 v58, v59, v59, 1.0
	v_rsq_f32_e32 v61, v58
	s_nop 0
	v_mul_f32_e32 v62, v61, v59
	v_mul_f32_e32 v55, v62, v54
	v_mul_f32_e32 v56, v62, v53
	v_fma_f32 v53, v61, v53, -v55
	v_fma_f32 v54, v61, v54, v56
	v_mul_f32_e32 v55, v52, v52
	v_mul_f32_e32 v56, v53, v53
	v_mul_f32_e32 v57, v52, v53
	v_add_f32_dpp v55, v55, v55 quad_perm:[1,0,3,2] row_mask:0xf bank_mask:0xf
	v_add_f32_dpp v56, v56, v56 quad_perm:[1,0,3,2] row_mask:0xf bank_mask:0xf
	v_add_f32_dpp v57, v57, v57 quad_perm:[1,0,3,2] row_mask:0xf bank_mask:0xf
	v_add_f32_dpp v55, v55, v55 quad_perm:[2,3,0,1] row_mask:0xf bank_mask:0xf
	v_add_f32_dpp v56, v56, v56 quad_perm:[2,3,0,1] row_mask:0xf bank_mask:0xf
	v_add_f32_dpp v57, v57, v57 quad_perm:[2,3,0,1] row_mask:0xf bank_mask:0xf
	v_sub_f32_e32 v60, v56, v55
	v_mul_f32_e32 v58, v57, v57
	v_cmp_gt_f32_e32 vcc, 0, v60
	v_mul_f32_e32 v59, v60, v60
	v_fmac_f32_e32 v59, 4.0, v58
	v_sqrt_f32_e32 v59, v59
	v_mul_f32_e32 v63, v62, v42
	v_mul_f32_e32 v43, v62, v41
	v_fma_f32 v41, v61, v41, -v63
	v_fma_f32 v42, v61, v42, v43
	v_add_f32_e64 v59, |v60|, v59
	v_add_f32_e32 v59, 0x0da24260, v59
	v_rcp_f32_e32 v59, v59
	v_add_f32_e32 v58, v57, v57
	v_mul_f32_e32 v59, v58, v59
	v_cndmask_b32_e64 v59, v59, -v59, vcc
	v_fma_f32 v58, v59, v59, 1.0
	v_rsq_f32_e32 v61, v58
	s_nop 0
	v_mul_f32_e32 v62, v61, v59
	v_mul_f32_e32 v55, v62, v53
	v_mul_f32_e32 v56, v62, v52
	v_fma_f32 v52, v61, v52, -v55
	v_fma_f32 v53, v61, v53, v56
	v_mul_f32_e32 v55, v52, v52
	v_mul_f32_e32 v56, v54, v54
	v_mul_f32_e32 v57, v52, v54
	v_add_f32_dpp v55, v55, v55 quad_perm:[1,0,3,2] row_mask:0xf bank_mask:0xf
	v_add_f32_dpp v56, v56, v56 quad_perm:[1,0,3,2] row_mask:0xf bank_mask:0xf
	v_add_f32_dpp v57, v57, v57 quad_perm:[1,0,3,2] row_mask:0xf bank_mask:0xf
	v_add_f32_dpp v55, v55, v55 quad_perm:[2,3,0,1] row_mask:0xf bank_mask:0xf
	v_add_f32_dpp v56, v56, v56 quad_perm:[2,3,0,1] row_mask:0xf bank_mask:0xf
	v_add_f32_dpp v57, v57, v57 quad_perm:[2,3,0,1] row_mask:0xf bank_mask:0xf
	v_sub_f32_e32 v60, v56, v55
	v_mul_f32_e32 v58, v57, v57
	v_cmp_gt_f32_e32 vcc, 0, v60
	v_mul_f32_e32 v59, v60, v60
	v_fmac_f32_e32 v59, 4.0, v58
	v_sqrt_f32_e32 v59, v59
	v_mul_f32_e32 v63, v62, v41
	v_mul_f32_e32 v43, v62, v40
	v_fma_f32 v40, v61, v40, -v63
	v_fma_f32 v41, v61, v41, v43
	v_add_f32_e64 v59, |v60|, v59
	v_add_f32_e32 v59, 0x0da24260, v59
	v_rcp_f32_e32 v59, v59
	v_add_f32_e32 v58, v57, v57
	v_mul_f32_e32 v59, v58, v59
	v_cndmask_b32_e64 v59, v59, -v59, vcc
	v_fma_f32 v58, v59, v59, 1.0
	v_rsq_f32_e32 v61, v58
	s_nop 0
	v_mul_f32_e32 v62, v61, v59
	v_mul_f32_e32 v55, v62, v54
	v_mul_f32_e32 v56, v62, v52
	v_fma_f32 v52, v61, v52, -v55
	v_fma_f32 v54, v61, v54, v56
	v_mul_f32_e32 v55, v53, v53
	v_mul_f32_e32 v56, v54, v54
	v_mul_f32_e32 v57, v53, v54
	v_add_f32_dpp v55, v55, v55 quad_perm:[1,0,3,2] row_mask:0xf bank_mask:0xf
	v_add_f32_dpp v56, v56, v56 quad_perm:[1,0,3,2] row_mask:0xf bank_mask:0xf
	v_add_f32_dpp v57, v57, v57 quad_perm:[1,0,3,2] row_mask:0xf bank_mask:0xf
	v_add_f32_dpp v55, v55, v55 quad_perm:[2,3,0,1] row_mask:0xf bank_mask:0xf
	v_add_f32_dpp v56, v56, v56 quad_perm:[2,3,0,1] row_mask:0xf bank_mask:0xf
	v_add_f32_dpp v57, v57, v57 quad_perm:[2,3,0,1] row_mask:0xf bank_mask:0xf
	v_sub_f32_e32 v60, v56, v55
	v_mul_f32_e32 v58, v57, v57
	v_cmp_gt_f32_e32 vcc, 0, v60
	v_mul_f32_e32 v59, v60, v60
	v_fmac_f32_e32 v59, 4.0, v58
	v_sqrt_f32_e32 v59, v59
	v_mul_f32_e32 v63, v62, v42
	v_mul_f32_e32 v43, v62, v40
	v_fma_f32 v40, v61, v40, -v63
	v_fma_f32 v42, v61, v42, v43
	v_add_f32_e64 v59, |v60|, v59
	v_add_f32_e32 v59, 0x0da24260, v59
	v_rcp_f32_e32 v59, v59
	v_add_f32_e32 v58, v57, v57
	v_mul_f32_e32 v59, v58, v59
	v_cndmask_b32_e64 v59, v59, -v59, vcc
	v_fma_f32 v58, v59, v59, 1.0
	v_rsq_f32_e32 v61, v58
	s_nop 0
	v_mul_f32_e32 v62, v61, v59
	v_mul_f32_e32 v55, v62, v54
	v_mul_f32_e32 v56, v62, v53
	v_fma_f32 v53, v61, v53, -v55
	v_fma_f32 v54, v61, v54, v56
	v_mul_f32_e32 v55, v52, v52
	v_mul_f32_e32 v56, v53, v53
	v_mul_f32_e32 v57, v52, v53
	v_add_f32_dpp v55, v55, v55 quad_perm:[1,0,3,2] row_mask:0xf bank_mask:0xf
	v_add_f32_dpp v56, v56, v56 quad_perm:[1,0,3,2] row_mask:0xf bank_mask:0xf
	v_add_f32_dpp v57, v57, v57 quad_perm:[1,0,3,2] row_mask:0xf bank_mask:0xf
	v_add_f32_dpp v55, v55, v55 quad_perm:[2,3,0,1] row_mask:0xf bank_mask:0xf
	v_add_f32_dpp v56, v56, v56 quad_perm:[2,3,0,1] row_mask:0xf bank_mask:0xf
	v_add_f32_dpp v57, v57, v57 quad_perm:[2,3,0,1] row_mask:0xf bank_mask:0xf
	v_sub_f32_e32 v60, v56, v55
	v_mul_f32_e32 v58, v57, v57
	v_cmp_gt_f32_e32 vcc, 0, v60
	v_mul_f32_e32 v59, v60, v60
	v_fmac_f32_e32 v59, 4.0, v58
	v_sqrt_f32_e32 v59, v59
	v_mul_f32_e32 v63, v62, v42
	v_mul_f32_e32 v43, v62, v41
	v_fma_f32 v41, v61, v41, -v63
	v_fma_f32 v42, v61, v42, v43
	v_add_f32_e64 v59, |v60|, v59
	v_add_f32_e32 v59, 0x0da24260, v59
	v_rcp_f32_e32 v59, v59
	v_add_f32_e32 v58, v57, v57
	v_mul_f32_e32 v59, v58, v59
	v_cndmask_b32_e64 v59, v59, -v59, vcc
	v_fma_f32 v58, v59, v59, 1.0
	v_rsq_f32_e32 v61, v58
	s_nop 0
	v_mul_f32_e32 v62, v61, v59
	v_mul_f32_e32 v55, v62, v53
	v_mul_f32_e32 v56, v62, v52
	v_fma_f32 v52, v61, v52, -v55
	v_fma_f32 v53, v61, v53, v56
	v_mul_f32_e32 v55, v52, v52
	v_mul_f32_e32 v56, v54, v54
	v_mul_f32_e32 v57, v52, v54
	v_add_f32_dpp v55, v55, v55 quad_perm:[1,0,3,2] row_mask:0xf bank_mask:0xf
	v_add_f32_dpp v56, v56, v56 quad_perm:[1,0,3,2] row_mask:0xf bank_mask:0xf
	v_add_f32_dpp v57, v57, v57 quad_perm:[1,0,3,2] row_mask:0xf bank_mask:0xf
	v_add_f32_dpp v55, v55, v55 quad_perm:[2,3,0,1] row_mask:0xf bank_mask:0xf
	v_add_f32_dpp v56, v56, v56 quad_perm:[2,3,0,1] row_mask:0xf bank_mask:0xf
	v_add_f32_dpp v57, v57, v57 quad_perm:[2,3,0,1] row_mask:0xf bank_mask:0xf
	v_sub_f32_e32 v60, v56, v55
	v_mul_f32_e32 v58, v57, v57
	v_cmp_gt_f32_e32 vcc, 0, v60
	v_mul_f32_e32 v59, v60, v60
	v_fmac_f32_e32 v59, 4.0, v58
	v_sqrt_f32_e32 v59, v59
	v_mul_f32_e32 v63, v62, v41
	v_mul_f32_e32 v43, v62, v40
	v_fma_f32 v40, v61, v40, -v63
	v_fma_f32 v41, v61, v41, v43
	v_add_f32_e64 v59, |v60|, v59
	v_add_f32_e32 v59, 0x0da24260, v59
	v_rcp_f32_e32 v59, v59
	v_add_f32_e32 v58, v57, v57
	v_mul_f32_e32 v59, v58, v59
	v_cndmask_b32_e64 v59, v59, -v59, vcc
	v_fma_f32 v58, v59, v59, 1.0
	v_rsq_f32_e32 v61, v58
	s_nop 0
	v_mul_f32_e32 v62, v61, v59
	v_mul_f32_e32 v55, v62, v54
	v_mul_f32_e32 v56, v62, v52
	v_fma_f32 v52, v61, v52, -v55
	v_fma_f32 v54, v61, v54, v56
	v_mul_f32_e32 v55, v53, v53
	v_mul_f32_e32 v56, v54, v54
	v_mul_f32_e32 v57, v53, v54
	v_add_f32_dpp v55, v55, v55 quad_perm:[1,0,3,2] row_mask:0xf bank_mask:0xf
	v_add_f32_dpp v56, v56, v56 quad_perm:[1,0,3,2] row_mask:0xf bank_mask:0xf
	v_add_f32_dpp v57, v57, v57 quad_perm:[1,0,3,2] row_mask:0xf bank_mask:0xf
	v_add_f32_dpp v55, v55, v55 quad_perm:[2,3,0,1] row_mask:0xf bank_mask:0xf
	v_add_f32_dpp v56, v56, v56 quad_perm:[2,3,0,1] row_mask:0xf bank_mask:0xf
	v_add_f32_dpp v57, v57, v57 quad_perm:[2,3,0,1] row_mask:0xf bank_mask:0xf
	v_sub_f32_e32 v60, v56, v55
	v_mul_f32_e32 v58, v57, v57
	v_cmp_gt_f32_e32 vcc, 0, v60
	v_mul_f32_e32 v59, v60, v60
	v_fmac_f32_e32 v59, 4.0, v58
	v_sqrt_f32_e32 v59, v59
	v_mul_f32_e32 v63, v62, v42
	v_mul_f32_e32 v43, v62, v40
	v_fma_f32 v40, v61, v40, -v63
	v_fma_f32 v42, v61, v42, v43
	v_add_f32_e64 v59, |v60|, v59
	v_add_f32_e32 v59, 0x0da24260, v59
	v_rcp_f32_e32 v59, v59
	v_add_f32_e32 v58, v57, v57
	v_mul_f32_e32 v59, v58, v59
	v_cndmask_b32_e64 v59, v59, -v59, vcc
	v_fma_f32 v58, v59, v59, 1.0
	v_rsq_f32_e32 v61, v58
	s_nop 0
	v_mul_f32_e32 v62, v61, v59
	v_mul_f32_e32 v55, v62, v54
	v_mul_f32_e32 v56, v62, v53
	v_fma_f32 v53, v61, v53, -v55
	v_fma_f32 v54, v61, v54, v56
	v_mul_f32_e32 v63, v62, v42
	v_mul_f32_e32 v43, v62, v41
	v_fma_f32 v41, v61, v41, -v63
	v_fma_f32 v42, v61, v42, v43
	v_mul_f32_e32 v55, v52, v52
	v_mul_f32_e32 v56, v53, v53
	v_mul_f32_e32 v57, v54, v54
	v_add_f32_dpp v55, v55, v55 quad_perm:[1,0,3,2] row_mask:0xf bank_mask:0xf
	v_add_f32_dpp v56, v56, v56 quad_perm:[1,0,3,2] row_mask:0xf bank_mask:0xf
	v_add_f32_dpp v57, v57, v57 quad_perm:[1,0,3,2] row_mask:0xf bank_mask:0xf
	v_add_f32_dpp v55, v55, v55 quad_perm:[2,3,0,1] row_mask:0xf bank_mask:0xf
	v_add_f32_dpp v56, v56, v56 quad_perm:[2,3,0,1] row_mask:0xf bank_mask:0xf
	v_add_f32_dpp v57, v57, v57 quad_perm:[2,3,0,1] row_mask:0xf bank_mask:0xf
	v_cmp_le_f32_e64 s[28:29], v55, v56
	v_cmp_le_f32_e64 s[30:31], v55, v57
	v_cmp_lt_f32_e32 vcc, v57, v56
	s_and_b64 s[28:29], s[28:29], s[30:31]
	s_andn2_b64 s[30:31], vcc, s[28:29]
	v_cndmask_b32_e64 v44, v52, v53, s[28:29]
	v_cndmask_b32_e64 v45, v54, v53, s[30:31]
	v_cndmask_b32_e64 v46, v40, v41, s[28:29]
	v_cndmask_b32_e64 v47, v42, v41, s[30:31]
	v_mul_f32_e32 v58, v44, v44
	s_nop 1
	v_add_f32_dpp v58, v58, v58 quad_perm:[1,0,3,2] row_mask:0xf bank_mask:0xf
	s_nop 1
	v_add_f32_dpp v58, v58, v58 quad_perm:[2,3,0,1] row_mask:0xf bank_mask:0xf
	v_max_f32_e32 v58, 0x3aa2425, v58
	v_rsq_f32_e32 v58, v58
	s_nop 0
	v_mul_f32_e32 v48, v44, v58
	v_mul_f32_e32 v59, v48, v45
	s_nop 1
	v_add_f32_dpp v59, v59, v59 quad_perm:[1,0,3,2] row_mask:0xf bank_mask:0xf
	s_nop 1
	v_add_f32_dpp v59, v59, v59 quad_perm:[2,3,0,1] row_mask:0xf bank_mask:0xf
	v_fma_f32 v49, -v59, v48, v45
	v_mul_f32_e32 v58, v49, v49
	s_nop 1
	v_add_f32_dpp v58, v58, v58 quad_perm:[1,0,3,2] row_mask:0xf bank_mask:0xf
	s_nop 1
	v_add_f32_dpp v58, v58, v58 quad_perm:[2,3,0,1] row_mask:0xf bank_mask:0xf
	v_max_f32_e32 v58, 0x3aa2425, v58
	v_rsq_f32_e32 v58, v58
	s_nop 0
	v_mul_f32_e32 v50, v49, v58
	v_mov_b32_dpp v43, v47 quad_perm:[2,0,1,3] row_mask:0xf bank_mask:0xf
	v_mov_b32_dpp v63, v47 quad_perm:[1,2,0,3] row_mask:0xf bank_mask:0xf
	v_mov_b32_dpp v62, v50 quad_perm:[2,0,1,3] row_mask:0xf bank_mask:0xf
	v_mov_b32_dpp v61, v50 quad_perm:[1,2,0,3] row_mask:0xf bank_mask:0xf
	v_mul_f32_dpp v60, v46, v43 quad_perm:[1,2,0,3] row_mask:0xf bank_mask:0xf
	v_mul_f32_dpp v51, v48, v62 quad_perm:[1,2,0,3] row_mask:0xf bank_mask:0xf
	s_nop 0
	v_fmac_f32_dpp v60, -v46, v63 quad_perm:[2,0,1,3] row_mask:0xf bank_mask:0xf
	v_fmac_f32_dpp v51, -v48, v61 quad_perm:[2,0,1,3] row_mask:0xf bank_mask:0xf
	v_mul_f32_dpp v52, v46, v48 quad_perm:[0,0,0,0] row_mask:0xf bank_mask:0xf
	v_mul_f32_dpp v53, v46, v48 quad_perm:[1,1,1,1] row_mask:0xf bank_mask:0xf
	v_mul_f32_dpp v54, v46, v48 quad_perm:[2,2,2,2] row_mask:0xf bank_mask:0xf
	v_fmac_f32_dpp v52, v47, v50 quad_perm:[0,0,0,0] row_mask:0xf bank_mask:0xf
	v_fmac_f32_dpp v53, v47, v50 quad_perm:[1,1,1,1] row_mask:0xf bank_mask:0xf
	v_fmac_f32_dpp v54, v47, v50 quad_perm:[2,2,2,2] row_mask:0xf bank_mask:0xf
	v_fmac_f32_dpp v52, v60, v51 quad_perm:[0,0,0,0] row_mask:0xf bank_mask:0xf
	v_fmac_f32_dpp v53, v60, v51 quad_perm:[1,1,1,1] row_mask:0xf bank_mask:0xf
	v_fmac_f32_dpp v54, v60, v51 quad_perm:[2,2,2,2] row_mask:0xf bank_mask:0xf
	v_mov_b32_e32 v55, 0
	v_writelane_b32 v55, s32, 48
	v_writelane_b32 v55, s33, 49
	v_writelane_b32 v55, s34, 50
	v_mul_f32_e32 v55, 0xbc800000, v55
	v_mul_f32_e32 v56, v55, v52
	v_mul_f32_e32 v57, v55, v53
	v_mul_f32_e32 v58, v55, v54
	v_add_f32_dpp v56, v56, v56 quad_perm:[1,0,3,2] row_mask:0xf bank_mask:0xf
	v_add_f32_dpp v57, v57, v57 quad_perm:[1,0,3,2] row_mask:0xf bank_mask:0xf
	v_add_f32_dpp v58, v58, v58 quad_perm:[1,0,3,2] row_mask:0xf bank_mask:0xf
	v_add_f32_dpp v56, v56, v56 quad_perm:[2,3,0,1] row_mask:0xf bank_mask:0xf
	v_add_f32_dpp v57, v57, v57 quad_perm:[2,3,0,1] row_mask:0xf bank_mask:0xf
	v_add_f32_dpp v58, v58, v58 quad_perm:[2,3,0,1] row_mask:0xf bank_mask:0xf
	v_cndmask_b32_e64 v52, v52, v56, s[26:27]
	v_cndmask_b32_e64 v53, v53, v57, s[26:27]
	v_cndmask_b32_e64 v54, v54, v58, s[26:27]
	v_subrev_u32_e32 v59, 48, v0
	v_lshlrev_b32_e32 v59, 4, v59
	s_mov_b32 s20, 0
	s_mov_b32 s21, 0xf0000
	s_mov_b64 exec, s[20:21]
	ds_write_b96 v59, v[52:54] offset:24576
	s_mov_b64 exec, -1
	s_waitcnt lgkmcnt(0)
	s_branch .Ljoin
.Lbulk_waves:
	global_load_dwordx4 v[8:11], v1, s[4:5] offset:-2048 nt
	global_load_dwordx4 v[12:15], v1, s[4:5] offset:-1024 nt
	global_load_dwordx4 v[16:19], v1, s[4:5] offset:0 nt
	global_load_dwordx4 v[20:23], v1, s[4:5] offset:1024 nt
	global_load_dwordx4 v[24:27], v1, s[4:5] offset:2048 nt
	s_and_saveexec_b64 s[16:17], s[14:15]
	global_load_dwordx4 v[28:31], v1, s[4:5] offset:3072 nt
	s_mov_b64 exec, s[16:17]
	s_waitcnt vmcnt(0)
	ds_write_b128 v2, v[8:11]
	ds_write_b128 v2, v[12:15] offset:1024
	ds_write_b128 v2, v[16:19] offset:2048
	ds_write_b128 v2, v[20:23] offset:3072
	ds_write_b128 v2, v[24:27] offset:4096
	ds_write_b128 v2, v[28:31] offset:5120
	s_waitcnt lgkmcnt(0)
	s_barrier
.Ljoin:
	s_barrier
	v_mov_b32_e32 v6, 0x6000
	ds_read_b96 v[32:34], v6
	ds_read_b96 v[36:38], v6 offset:16
	ds_read_b96 v[40:42], v6 offset:32
	ds_read_b96 v[44:46], v6 offset:48
	v_add_u32_e32 v56, 0xc00, v3
	v_add_u32_e32 v57, 0x1200, v3
	ds_read2_b32 v[8:9], v3 offset0:0 offset1:1
	ds_read_b32 v24, v3 offset:8
	ds_read2_b32 v[10:11], v3 offset0:192 offset1:193
	ds_read_b32 v25, v3 offset:776
	ds_read2_b32 v[12:13], v4 offset0:0 offset1:1
	ds_read_b32 v26, v4 offset:8
	s_waitcnt lgkmcnt(4)
	v_fma_f32 v60, v8, v32, v44
	v_fma_f32 v61, v8, v33, v45
	v_fma_f32 v62, v8, v34, v46
	v_fmac_f32_e32 v60, v9, v36
	v_fmac_f32_e32 v61, v9, v37
	v_fmac_f32_e32 v62, v9, v38
	v_fmac_f32_e32 v60, v24, v40
	v_fmac_f32_e32 v61, v24, v41
	v_fmac_f32_e32 v62, v24, v42
	ds_write2_b32 v3, v60, v61 offset0:0 offset1:1
	ds_write_b32 v3, v62 offset:8
	ds_read2_b32 v[14:15], v4 offset0:192 offset1:193
	ds_read_b32 v27, v4 offset:776
	s_waitcnt lgkmcnt(6)
	v_fma_f32 v35, v10, v32, v44
	v_fma_f32 v39, v10, v33, v45
	v_fma_f32 v43, v10, v34, v46
	v_fmac_f32_e32 v35, v11, v36
	v_fmac_f32_e32 v39, v11, v37
	v_fmac_f32_e32 v43, v11, v38
	v_fmac_f32_e32 v35, v25, v40
	v_fmac_f32_e32 v39, v25, v41
	v_fmac_f32_e32 v43, v25, v42
	ds_write2_b32 v3, v35, v39 offset0:192 offset1:193
	ds_write_b32 v3, v43 offset:776
	ds_read2_b32 v[16:17], v56 offset0:0 offset1:1
	ds_read_b32 v28, v56 offset:8
	s_waitcnt lgkmcnt(8)
	v_fma_f32 v60, v12, v32, v44
	v_fma_f32 v61, v12, v33, v45
	v_fma_f32 v62, v12, v34, v46
	v_fmac_f32_e32 v60, v13, v36
	v_fmac_f32_e32 v61, v13, v37
	v_fmac_f32_e32 v62, v13, v38
	v_fmac_f32_e32 v60, v26, v40
	v_fmac_f32_e32 v61, v26, v41
	v_fmac_f32_e32 v62, v26, v42
	ds_write2_b32 v4, v60, v61 offset0:0 offset1:1
	ds_write_b32 v4, v62 offset:8
	ds_read2_b32 v[18:19], v56 offset0:192 offset1:193
	ds_read_b32 v29, v56 offset:776
	s_waitcnt lgkmcnt(8)
	v_fma_f32 v35, v14, v32, v44
	v_fma_f32 v39, v14, v33, v45
	v_fma_f32 v43, v14, v34, v46
	v_fmac_f32_e32 v35, v15, v36
	v_fmac_f32_e32 v39, v15, v37
	v_fmac_f32_e32 v43, v15, v38
	v_fmac_f32_e32 v35, v27, v40
	v_fmac_f32_e32 v39, v27, v41
	v_fmac_f32_e32 v43, v27, v42
	ds_write2_b32 v4, v35, v39 offset0:192 offset1:193
	ds_write_b32 v4, v43 offset:776
	ds_read2_b32 v[20:21], v57 offset0:0 offset1:1
	ds_read_b32 v30, v57 offset:8
	s_waitcnt lgkmcnt(8)
	v_fma_f32 v60, v16, v32, v44
	v_fma_f32 v61, v16, v33, v45
	v_fma_f32 v62, v16, v34, v46
	v_fmac_f32_e32 v60, v17, v36
	v_fmac_f32_e32 v61, v17, v37
	v_fmac_f32_e32 v62, v17, v38
	v_fmac_f32_e32 v60, v28, v40
	v_fmac_f32_e32 v61, v28, v41
	v_fmac_f32_e32 v62, v28, v42
	ds_write2_b32 v56, v60, v61 offset0:0 offset1:1
	ds_write_b32 v56, v62 offset:8
	ds_read2_b32 v[22:23], v57 offset0:192 offset1:193
	ds_read_b32 v31, v57 offset:776
	s_waitcnt lgkmcnt(8)
	v_fma_f32 v35, v18, v32, v44
	v_fma_f32 v39, v18, v33, v45
	v_fma_f32 v43, v18, v34, v46
	v_fmac_f32_e32 v35, v19, v36
	v_fmac_f32_e32 v39, v19, v37
	v_fmac_f32_e32 v43, v19, v38
	v_fmac_f32_e32 v35, v29, v40
	v_fmac_f32_e32 v39, v29, v41
	v_fmac_f32_e32 v43, v29, v42
	ds_write2_b32 v56, v35, v39 offset0:192 offset1:193
	ds_write_b32 v56, v43 offset:776
	s_waitcnt lgkmcnt(6)
	v_fma_f32 v60, v20, v32, v44
	v_fma_f32 v61, v20, v33, v45
	v_fma_f32 v62, v20, v34, v46
	v_fmac_f32_e32 v60, v21, v36
	v_fmac_f32_e32 v61, v21, v37
	v_fmac_f32_e32 v62, v21, v38
	v_fmac_f32_e32 v60, v30, v40
	v_fmac_f32_e32 v61, v30, v41
	v_fmac_f32_e32 v62, v30, v42
	ds_write2_b32 v57, v60, v61 offset0:0 offset1:1
	ds_write_b32 v57, v62 offset:8
	s_waitcnt lgkmcnt(4)
	v_fma_f32 v35, v22, v32, v44
	v_fma_f32 v39, v22, v33, v45
	v_fma_f32 v43, v22, v34, v46
	v_fmac_f32_e32 v35, v23, v36
	v_fmac_f32_e32 v39, v23, v37
	v_fmac_f32_e32 v43, v23, v38
	v_fmac_f32_e32 v35, v31, v40
	v_fmac_f32_e32 v39, v31, v41
	v_fmac_f32_e32 v43, v31, v42
	ds_write2_b32 v57, v35, v39 offset0:192 offset1:193
	ds_write_b32 v57, v43 offset:776
	ds_read_b128 v[8:11], v2
	ds_read_b128 v[12:15], v2 offset:1024
	ds_read_b128 v[16:19], v2 offset:2048
	ds_read_b128 v[20:23], v2 offset:3072
	ds_read_b128 v[24:27], v2 offset:4096
	ds_read_b128 v[28:31], v2 offset:5120
	s_waitcnt lgkmcnt(5)
	global_store_dwordx4 v1, v[8:11], s[10:11] offset:-2048 sc0 sc1
	s_waitcnt lgkmcnt(4)
	global_store_dwordx4 v1, v[12:15], s[10:11] offset:-1024 sc0 sc1
	s_waitcnt lgkmcnt(3)
	global_store_dwordx4 v1, v[16:19], s[10:11] offset:0 sc0 sc1
	s_waitcnt lgkmcnt(2)
	global_store_dwordx4 v1, v[20:23], s[10:11] offset:1024 sc0 sc1
	s_waitcnt lgkmcnt(1)
	global_store_dwordx4 v1, v[24:27], s[10:11] offset:2048 sc0 sc1
	s_waitcnt lgkmcnt(0)
	s_and_saveexec_b64 s[16:17], s[14:15]
	global_store_dwordx4 v1, v[28:31], s[10:11] offset:3072 sc0 sc1
	s_endpgm

	.amdhsa_kernel _Z11align_fusedPKfS0_PKiPf
		.amdhsa_group_segment_fixed_size 24640
		.amdhsa_private_segment_fixed_size 0
		.amdhsa_kernarg_size 32
		.amdhsa_user_sgpr_count 2
		.amdhsa_user_sgpr_dispatch_ptr 0
		.amdhsa_user_sgpr_queue_ptr 0
		.amdhsa_user_sgpr_kernarg_segment_ptr 1
		.amdhsa_user_sgpr_dispatch_id 0
		.amdhsa_user_sgpr_kernarg_preload_length 0
		.amdhsa_user_sgpr_kernarg_preload_offset 0
		.amdhsa_user_sgpr_private_segment_size 0
		.amdhsa_uses_dynamic_stack 0
		.amdhsa_enable_private_segment 0
		.amdhsa_system_sgpr_workgroup_id_x 1
		.amdhsa_system_sgpr_workgroup_id_y 0
		.amdhsa_system_sgpr_workgroup_id_z 0
		.amdhsa_system_sgpr_workgroup_info 0
		.amdhsa_system_vgpr_workitem_id 0
		.amdhsa_next_free_vgpr 64
		.amdhsa_next_free_sgpr 48
		.amdhsa_accum_offset 64
		.amdhsa_reserve_vcc 1
		.amdhsa_float_round_mode_32 0
		.amdhsa_float_round_mode_16_64 0
		.amdhsa_float_denorm_mode_32 3
		.amdhsa_float_denorm_mode_16_64 3
		.amdhsa_dx10_clamp 1
		.amdhsa_ieee_mode 1
		.amdhsa_fp16_overflow 0
		.amdhsa_tg_split 0
		.amdhsa_exception_fp_ieee_invalid_op 0
		.amdhsa_exception_fp_denorm_src 0
		.amdhsa_exception_fp_ieee_div_zero 0
		.amdhsa_exception_fp_ieee_overflow 0
		.amdhsa_exception_fp_ieee_underflow 0
		.amdhsa_exception_fp_ieee_inexact 0
		.amdhsa_exception_int_div_zero 0
	.end_amdhsa_kernel

.Lfunc_end0:
	.size	_Z11align_fusedPKfS0_PKiPf, .Lfunc_end0-_Z11align_fusedPKfS0_PKiPf
	.set _Z11align_fusedPKfS0_PKiPf.num_vgpr, 64
	.set _Z11align_fusedPKfS0_PKiPf.num_agpr, 0
	.set _Z11align_fusedPKfS0_PKiPf.numbered_sgpr, 48
	.set _Z11align_fusedPKfS0_PKiPf.num_named_barrier, 0
	.set _Z11align_fusedPKfS0_PKiPf.private_seg_size, 0
	.set _Z11align_fusedPKfS0_PKiPf.uses_vcc, 1
	.set _Z11align_fusedPKfS0_PKiPf.uses_flat_scratch, 0
	.set _Z11align_fusedPKfS0_PKiPf.has_dyn_sized_stack, 0
	.set _Z11align_fusedPKfS0_PKiPf.has_recursion, 0
	.set _Z11align_fusedPKfS0_PKiPf.has_indirect_call, 0

amdhsa.kernels:
  - .agpr_count:     0
    .args:
      - .actual_access:  read_only
        .address_space:  global
        .offset:         0
        .size:           8
        .value_kind:     global_buffer
      - .actual_access:  read_only
        .address_space:  global
        .offset:         8
        .size:           8
        .value_kind:     global_buffer
      - .actual_access:  read_only
        .address_space:  global
        .offset:         16
        .size:           8
        .value_kind:     global_buffer
      - .actual_access:  write_only
        .address_space:  global
        .offset:         24
        .size:           8
        .value_kind:     global_buffer
    .group_segment_fixed_size: 24640
    .kernarg_segment_align: 8
    .kernarg_segment_size: 32
    .language:       OpenCL C
    .language_version:
      - 2
      - 0
    .max_flat_workgroup_size: 256
    .name:           _Z11align_fusedPKfS0_PKiPf
    .private_segment_fixed_size: 0
    .sgpr_count:     54
    .sgpr_spill_count: 0
    .symbol:         _Z11align_fusedPKfS0_PKiPf.kd
    .uniform_work_group_size: 1
    .uses_dynamic_stack: false
    .vgpr_count:     64
    .vgpr_spill_count: 0
    .wavefront_size: 64
